# stream: chunk 0 and chunk 1 roles swapped statically (loads ascending within a row); early barrier + rotated wave-row kept
# speedup vs baseline: 1.0313x; 1.0022x over previous
.LBB1_2:
	s_or_b64 exec, exec, s[0:1]
	s_lshr_b32 s8, s3, 6
	s_add_i32 s8, s8, s2
	s_and_b32 s8, s8, 15
	s_lshl_b32 s0, s2, 7
	v_and_b32_e32 v24, 63, v0
	s_add_i32 s9, s8, s0
	s_waitcnt lgkmcnt(0)
	s_and_b32 s1, s5, 0xffff
	s_mov_b32 s3, 0x20000
	s_brev_b32 s2, 16
	s_mov_b32 s0, s4
	v_lshlrev_b32_e32 v25, 4, v24
	s_lshl_b32 s4, s9, 12
	buffer_load_dwordx4 v[26:29], v25, s[0:3], s4 offen nt
	buffer_load_dwordx4 v[30:33], v25, s[0:3], s4 offen offset:1024 nt
	buffer_load_dwordx4 v[34:37], v25, s[0:3], s4 offen offset:2048 nt
	s_barrier
	s_add_i32 s5, s4, 0x10000
	buffer_load_dwordx4 v[38:41], v25, s[0:3], s5 offen nt
	buffer_load_dwordx4 v[42:45], v25, s[0:3], s5 offen offset:1024 nt
	buffer_load_dwordx4 v[16:19], v25, s[0:3], s4 offen offset:3072 nt
	s_add_i32 s10, s4, 0x20000
	buffer_load_dwordx4 v[46:49], v25, s[0:3], s5 offen offset:2048 nt
	buffer_load_dwordx4 v[20:23], v25, s[0:3], s5 offen offset:3072 nt
	buffer_load_dwordx4 v[50:53], v25, s[0:3], s10 offen nt
	buffer_load_dwordx4 v[54:57], v25, s[0:3], s10 offen offset:1024 nt
	ds_read_b128 v[4:7], v25
	ds_read_b128 v[0:3], v25 offset:1024
	ds_read_b128 v[12:15], v25 offset:2048
	ds_read_b128 v[8:11], v25 offset:3072
	s_add_i32 s5, s4, 0x30000
	v_cmp_gt_u32_e32 vcc, 8, v24
	s_waitcnt vmcnt(9) lgkmcnt(3)
	v_pk_mul_f32 v[28:29], v[6:7], v[28:29]
	v_pk_mul_f32 v[26:27], v[4:5], v[26:27]
	s_waitcnt vmcnt(8) lgkmcnt(2)
	v_pk_fma_f32 v[32:33], v[2:3], v[32:33], v[28:29]
	v_pk_fma_f32 v[30:31], v[0:1], v[30:31], v[26:27]
	buffer_load_dwordx4 v[26:29], v25, s[0:3], s5 offen nt
	s_waitcnt vmcnt(8) lgkmcnt(1)
	v_pk_fma_f32 v[58:59], v[14:15], v[36:37], v[32:33]
	v_pk_fma_f32 v[60:61], v[12:13], v[34:35], v[30:31]
	buffer_load_dwordx4 v[30:33], v25, s[0:3], s5 offen offset:1024 nt
	s_waitcnt vmcnt(8)
	v_pk_mul_f32 v[34:35], v[6:7], v[40:41]
	v_pk_mul_f32 v[36:37], v[4:5], v[38:39]
	s_waitcnt vmcnt(7)
	v_pk_fma_f32 v[44:45], v[2:3], v[44:45], v[34:35]
	v_pk_fma_f32 v[42:43], v[0:1], v[42:43], v[36:37]
	buffer_load_dwordx4 v[34:37], v25, s[0:3], s10 offen offset:2048 nt
	s_waitcnt vmcnt(4)
	v_pk_mul_f32 v[38:39], v[6:7], v[52:53]
	v_pk_mul_f32 v[40:41], v[4:5], v[50:51]
	s_waitcnt vmcnt(3)
	v_pk_fma_f32 v[50:51], v[2:3], v[56:57], v[38:39]
	v_pk_fma_f32 v[52:53], v[0:1], v[54:55], v[40:41]
	buffer_load_dwordx4 v[38:41], v25, s[0:3], s10 offen offset:3072 nt
	v_pk_fma_f32 v[48:49], v[14:15], v[48:49], v[44:45]
	v_pk_fma_f32 v[46:47], v[12:13], v[46:47], v[42:43]
	s_waitcnt lgkmcnt(0)
	v_pk_fma_f32 v[18:19], v[10:11], v[18:19], v[58:59]
	v_pk_fma_f32 v[16:17], v[8:9], v[16:17], v[60:61]
	v_add_f32_e32 v61, v18, v19
	v_add_f32_e32 v60, v16, v17
	v_pk_fma_f32 v[16:17], v[10:11], v[22:23], v[48:49]
	v_pk_fma_f32 v[18:19], v[8:9], v[20:21], v[46:47]
	v_add_f32_e32 v16, v16, v17
	v_add_f32_e32 v18, v18, v19
	v_add_f32_e32 v60, v60, v61
	v_add_f32_e32 v16, v18, v16
	s_add_i32 s10, s4, 0x50000
	s_waitcnt vmcnt(3)
	v_pk_mul_f32 v[28:29], v[6:7], v[28:29]
	v_pk_mul_f32 v[26:27], v[4:5], v[26:27]
	v_add_f32_dpp v16, v16, v16 quad_perm:[1,0,3,2] row_mask:0xf bank_mask:0xf bound_ctrl:1
	s_waitcnt vmcnt(2)
	v_pk_fma_f32 v[54:55], v[2:3], v[32:33], v[28:29]
	v_pk_fma_f32 v[56:57], v[0:1], v[30:31], v[26:27]
	buffer_load_dwordx4 v[26:29], v25, s[0:3], s5 offen offset:2048 nt
	buffer_load_dwordx4 v[30:33], v25, s[0:3], s5 offen offset:3072 nt
	s_add_i32 s5, s4, 0x40000
	buffer_load_dwordx4 v[42:45], v25, s[0:3], s5 offen nt
	s_waitcnt vmcnt(4)
	v_pk_fma_f32 v[50:51], v[14:15], v[36:37], v[50:51]
	v_pk_fma_f32 v[52:53], v[12:13], v[34:35], v[52:53]
	buffer_load_dwordx4 v[34:37], v25, s[0:3], s5 offen offset:1024 nt
	v_add_f32_dpp v16, v16, v16 quad_perm:[2,3,0,1] row_mask:0xf bank_mask:0xf bound_ctrl:1
	s_waitcnt vmcnt(4)
	v_pk_fma_f32 v[58:59], v[10:11], v[40:41], v[50:51]
	v_pk_fma_f32 v[38:39], v[8:9], v[38:39], v[52:53]
	v_add_f32_e32 v19, v58, v59
	v_add_f32_e32 v17, v38, v39
	v_add_f32_dpp v58, v60, v60 quad_perm:[1,0,3,2] row_mask:0xf bank_mask:0xf bound_ctrl:1
	v_add_f32_e32 v18, v17, v19
	v_add_f32_dpp v16, v16, v16 row_ror:4 row_mask:0xf bank_mask:0xf bound_ctrl:1
	v_add_f32_dpp v17, v58, v58 quad_perm:[2,3,0,1] row_mask:0xf bank_mask:0xf bound_ctrl:1
	buffer_load_dwordx4 v[20:23], v25, s[0:3], s5 offen offset:2048 nt
	buffer_load_dwordx4 v[46:49], v25, s[0:3], s5 offen offset:3072 nt
	v_add_f32_dpp v17, v17, v17 row_ror:4 row_mask:0xf bank_mask:0xf bound_ctrl:1
	v_add_f32_dpp v58, v16, v16 row_ror:8 row_mask:0xf bank_mask:0xf bound_ctrl:1
	buffer_load_dwordx4 v[38:41], v25, s[0:3], s10 offen offset:1024 nt
	buffer_load_dwordx4 v[50:53], v25, s[0:3], s10 offen nt
	v_add_f32_dpp v17, v17, v17 row_ror:8 row_mask:0xf bank_mask:0xf bound_ctrl:1
	v_mov_b32_e32 v19, v17
	v_mov_b32_e32 v59, v58
	s_nop 0
	v_permlane16_swap_b32_e32 v17, v19
	v_permlane16_swap_b32_e32 v58, v59
	v_add_f32_e32 v16, v17, v19
	v_add_f32_e32 v17, v58, v59
	s_add_i32 s5, s4, 0x60000
	s_add_i32 s4, s4, 0x70000
	v_add_f32_dpp v18, v18, v18 quad_perm:[1,0,3,2] row_mask:0xf bank_mask:0xf bound_ctrl:1
	s_waitcnt vmcnt(7)
	v_pk_fma_f32 v[28:29], v[14:15], v[28:29], v[54:55]
	v_pk_fma_f32 v[54:55], v[12:13], v[26:27], v[56:57]
	s_waitcnt vmcnt(6)
	v_pk_fma_f32 v[58:59], v[10:11], v[32:33], v[28:29]
	buffer_load_dwordx4 v[26:29], v25, s[0:3], s10 offen offset:2048 nt
	v_pk_fma_f32 v[54:55], v[8:9], v[30:31], v[54:55]
	buffer_load_dwordx4 v[30:33], v25, s[0:3], s10 offen offset:3072 nt
	v_add_f32_e32 v66, v54, v55
	s_waitcnt vmcnt(7)
	v_pk_mul_f32 v[54:55], v[6:7], v[44:45]
	v_pk_mul_f32 v[56:57], v[4:5], v[42:43]
	buffer_load_dwordx4 v[42:45], v25, s[0:3], s5 offen nt
	s_waitcnt vmcnt(7)
	v_pk_fma_f32 v[54:55], v[2:3], v[36:37], v[54:55]
	v_pk_fma_f32 v[56:57], v[0:1], v[34:35], v[56:57]
	buffer_load_dwordx4 v[34:37], v25, s[0:3], s5 offen offset:1024 nt
	v_add_f32_dpp v18, v18, v18 quad_perm:[2,3,0,1] row_mask:0xf bank_mask:0xf bound_ctrl:1
	s_waitcnt vmcnt(7)
	v_pk_fma_f32 v[22:23], v[14:15], v[22:23], v[54:55]
	v_pk_fma_f32 v[20:21], v[12:13], v[20:21], v[56:57]
	s_waitcnt vmcnt(6)
	v_pk_fma_f32 v[60:61], v[10:11], v[48:49], v[22:23]
	v_pk_fma_f32 v[22:23], v[8:9], v[46:47], v[20:21]
	s_waitcnt vmcnt(4)
	v_pk_mul_f32 v[54:55], v[4:5], v[50:51]
	v_pk_mul_f32 v[20:21], v[6:7], v[52:53]
	v_pk_fma_f32 v[38:39], v[0:1], v[38:39], v[54:55]
	buffer_load_dwordx4 v[46:49], v25, s[0:3], s5 offen offset:2048 nt
	buffer_load_dwordx4 v[50:53], v25, s[0:3], s5 offen offset:3072 nt
	v_pk_fma_f32 v[20:21], v[2:3], v[40:41], v[20:21]
	v_add_f32_e32 v23, v22, v23
	v_add_f32_dpp v18, v18, v18 row_ror:4 row_mask:0xf bank_mask:0xf bound_ctrl:1
	s_waitcnt vmcnt(5)
	v_pk_fma_f32 v[26:27], v[12:13], v[26:27], v[38:39]
	buffer_load_dwordx4 v[38:41], v25, s[0:3], s4 offen offset:1024 nt
	buffer_load_dwordx4 v[54:57], v25, s[0:3], s4 offen nt
	v_pk_fma_f32 v[20:21], v[14:15], v[28:29], v[20:21]
	s_waitcnt vmcnt(6)
	v_pk_fma_f32 v[30:31], v[8:9], v[30:31], v[26:27]
	v_pk_fma_f32 v[62:63], v[10:11], v[32:33], v[20:21]
	v_add_f32_dpp v18, v18, v18 row_ror:8 row_mask:0xf bank_mask:0xf bound_ctrl:1
	s_waitcnt vmcnt(5)
	v_pk_mul_f32 v[20:21], v[6:7], v[44:45]
	v_pk_mul_f32 v[26:27], v[4:5], v[42:43]
	buffer_load_dwordx4 v[42:45], v25, s[0:3], s4 offen offset:2048 nt
	s_waitcnt vmcnt(5)
	v_pk_fma_f32 v[64:65], v[0:1], v[34:35], v[26:27]
	buffer_load_dwordx4 v[32:35], v25, s[0:3], s4 offen offset:3072 nt
	v_add_f32_e32 v27, v60, v61
	v_add_f32_e32 v23, v23, v27
	v_pk_fma_f32 v[36:37], v[2:3], v[36:37], v[20:21]
	v_add_f32_e32 v20, v58, v59
	v_add_f32_dpp v23, v23, v23 quad_perm:[1,0,3,2] row_mask:0xf bank_mask:0xf bound_ctrl:1
	v_add_f32_e32 v20, v66, v20
	v_mov_b32_e32 v19, v18
	v_add_f32_dpp v23, v23, v23 quad_perm:[2,3,0,1] row_mask:0xf bank_mask:0xf bound_ctrl:1
	v_add_f32_dpp v20, v20, v20 quad_perm:[1,0,3,2] row_mask:0xf bank_mask:0xf bound_ctrl:1
	v_permlane16_swap_b32_e32 v18, v19
	v_add_f32_dpp v23, v23, v23 row_ror:4 row_mask:0xf bank_mask:0xf bound_ctrl:1
	v_add_f32_dpp v20, v20, v20 quad_perm:[2,3,0,1] row_mask:0xf bank_mask:0xf bound_ctrl:1
	v_add_f32_e32 v18, v18, v19
	v_add_f32_dpp v23, v23, v23 row_ror:8 row_mask:0xf bank_mask:0xf bound_ctrl:1
	v_mov_b32_e32 v27, v23
	s_nop 1
	v_permlane16_swap_b32_e32 v23, v27
	v_add_f32_e32 v28, v23, v27
	v_add_f32_e32 v23, v30, v31
	s_waitcnt vmcnt(5)
	v_pk_fma_f32 v[30:31], v[14:15], v[48:49], v[36:37]
	v_pk_fma_f32 v[36:37], v[12:13], v[46:47], v[64:65]
	s_waitcnt vmcnt(4)
	v_pk_fma_f32 v[30:31], v[10:11], v[52:53], v[30:31]
	v_pk_fma_f32 v[36:37], v[8:9], v[50:51], v[36:37]
	v_add_f32_e32 v27, v62, v63
	v_add_f32_e32 v36, v36, v37
	v_add_f32_e32 v30, v30, v31
	v_add_f32_e32 v23, v23, v27
	v_add_f32_e32 v30, v36, v30
	v_add_f32_dpp v20, v20, v20 row_ror:4 row_mask:0xf bank_mask:0xf bound_ctrl:1
	v_add_f32_dpp v23, v23, v23 quad_perm:[1,0,3,2] row_mask:0xf bank_mask:0xf bound_ctrl:1
	v_add_f32_dpp v30, v30, v30 quad_perm:[1,0,3,2] row_mask:0xf bank_mask:0xf bound_ctrl:1
	v_add_f32_dpp v20, v20, v20 row_ror:8 row_mask:0xf bank_mask:0xf bound_ctrl:1
	v_add_f32_dpp v23, v23, v23 quad_perm:[2,3,0,1] row_mask:0xf bank_mask:0xf bound_ctrl:1
	v_add_f32_dpp v30, v30, v30 quad_perm:[2,3,0,1] row_mask:0xf bank_mask:0xf bound_ctrl:1
	v_mov_b32_e32 v21, v20
	v_add_f32_dpp v23, v23, v23 row_ror:4 row_mask:0xf bank_mask:0xf bound_ctrl:1
	v_add_f32_dpp v30, v30, v30 row_ror:4 row_mask:0xf bank_mask:0xf bound_ctrl:1
	v_permlane16_swap_b32_e32 v20, v21
	v_add_f32_dpp v23, v23, v23 row_ror:8 row_mask:0xf bank_mask:0xf bound_ctrl:1
	v_add_f32_dpp v30, v30, v30 row_ror:8 row_mask:0xf bank_mask:0xf bound_ctrl:1
	v_mov_b32_e32 v27, v23
	v_mov_b32_e32 v31, v30
	s_nop 0
	v_permlane16_swap_b32_e32 v23, v27
	v_permlane16_swap_b32_e32 v30, v31
	v_add_f32_e32 v21, v20, v21
	v_add_f32_e32 v23, v23, v27
	v_add_f32_e32 v30, v30, v31
	v_mov_b32_e32 v19, v16
	v_mov_b32_e32 v20, v17
	v_mov_b32_e32 v22, v18
	v_mov_b32_e32 v26, v21
	v_mov_b32_e32 v29, v28
	v_mov_b32_e32 v27, v23
	v_mov_b32_e32 v31, v30
	v_permlane32_swap_b32_e32 v16, v19
	v_permlane32_swap_b32_e32 v17, v20
	v_permlane32_swap_b32_e32 v18, v22
	v_permlane32_swap_b32_e32 v21, v26
	v_permlane32_swap_b32_e32 v28, v29
	v_permlane32_swap_b32_e32 v23, v27
	s_waitcnt vmcnt(2)
	v_pk_mul_f32 v[6:7], v[6:7], v[56:57]
	v_pk_mul_f32 v[4:5], v[4:5], v[54:55]
	v_pk_fma_f32 v[2:3], v[2:3], v[40:41], v[6:7]
	v_pk_fma_f32 v[0:1], v[0:1], v[38:39], v[4:5]
	v_permlane32_swap_b32_e32 v30, v31
	s_waitcnt vmcnt(1)
	v_pk_fma_f32 v[2:3], v[14:15], v[44:45], v[2:3]
	v_pk_fma_f32 v[0:1], v[12:13], v[42:43], v[0:1]
	s_waitcnt vmcnt(0)
	v_pk_fma_f32 v[2:3], v[10:11], v[34:35], v[2:3]
	v_pk_fma_f32 v[0:1], v[8:9], v[32:33], v[0:1]
	s_nop 0
	v_add_f32_e32 v0, v0, v1
	v_add_f32_e32 v1, v2, v3
	v_add_f32_e32 v0, v0, v1
	s_nop 1
	v_add_f32_dpp v0, v0, v0 quad_perm:[1,0,3,2] row_mask:0xf bank_mask:0xf bound_ctrl:1
	s_nop 1
	v_add_f32_dpp v0, v0, v0 quad_perm:[2,3,0,1] row_mask:0xf bank_mask:0xf bound_ctrl:1
	s_nop 1
	v_add_f32_dpp v0, v0, v0 row_ror:4 row_mask:0xf bank_mask:0xf bound_ctrl:1
	s_nop 1
	v_add_f32_dpp v0, v0, v0 row_ror:8 row_mask:0xf bank_mask:0xf bound_ctrl:1
	v_mov_b32_e32 v1, v0
	s_nop 1
	v_permlane16_swap_b32_e32 v0, v1
	v_add_f32_e32 v0, v0, v1
	v_mov_b32_e32 v1, v0
	s_nop 1
	v_permlane32_swap_b32_e32 v0, v1
	s_and_saveexec_b64 s[0:1], vcc
	s_cbranch_execz .LBB1_4
	v_add_f32_e32 v6, v16, v19
	v_cmp_eq_u32_e32 vcc, 0, v24
	v_add_f32_e32 v5, v17, v20
	v_add_f32_e32 v4, v18, v22
	v_cndmask_b32_e32 v6, 0, v6, vcc
	v_cmp_eq_u32_e32 vcc, 1, v24
	v_add_f32_e32 v3, v21, v26
	v_add_f32_e32 v2, v28, v29
	v_cndmask_b32_e32 v5, v6, v5, vcc
	v_cmp_eq_u32_e32 vcc, 2, v24
	v_add_f32_e32 v0, v0, v1
	v_add_f32_e32 v1, v30, v31
	v_cndmask_b32_e32 v4, v5, v4, vcc
	v_cmp_eq_u32_e32 vcc, 3, v24
	s_lshl_b32 s0, s8, 13
	s_and_b32 s0, s0, 0x1e000
	v_cndmask_b32_e32 v3, v4, v3, vcc
	v_cmp_eq_u32_e32 vcc, 4, v24
	s_add_u32 s0, s6, s0
	s_addc_u32 s1, s7, 0
	v_cndmask_b32_e32 v2, v3, v2, vcc
	v_add_f32_e32 v3, v23, v27
	v_cmp_eq_u32_e32 vcc, 5, v24
	s_nop 1
	v_cndmask_b32_e32 v2, v2, v3, vcc
	v_cmp_eq_u32_e32 vcc, 6, v24
	s_nop 1
	v_cndmask_b32_e32 v1, v2, v1, vcc
	v_cmp_eq_u32_e32 vcc, 7, v24
	s_nop 1
	v_cndmask_b32_e32 v2, v1, v0, vcc
	v_add_u32_e32 v0, s9, v25
	v_ashrrev_i32_e32 v0, 4, v0
	v_ashrrev_i32_e32 v1, 31, v0
	v_lshl_add_u64 v[0:1], v[0:1], 2, s[0:1]
	v_add_co_u32_e32 v0, vcc, 0x6000, v0
	s_nop 1
	v_addc_co_u32_e32 v1, vcc, 0, v1, vcc
	global_store_dword v[0:1], v2, off offset:64
